# MoE GEMM1 K-loop: A(0,0) LDS-DMA stage moved from load segment B to C (2/6/2/6 -> 2/4/4/6 pieces), segment B wait vmcnt(8)->vmcnt(6)
# baseline (speedup 1.0000x reference)
.LBB0_2336:
	ds_read_b128 v[106:109], v154
	ds_read_b128 v[110:113], v154 offset:1024
	ds_read_b128 v[138:141], v154 offset:2048
	ds_read_b128 v[142:145], v154 offset:3072
	ds_read_b128 v[162:165], v155
	ds_read_b128 v[166:169], v155 offset:1024
	ds_read_b128 v[170:173], v155 offset:2048
	ds_read_b128 v[174:177], v155 offset:3072
	s_add_i32 s65, s62, 0xfffa0080
	s_cmp_eq_u32 s64, 12
	s_cselect_b32 s65, s26, s65
	s_cselect_b32 s67, s27, s63
	s_add_i32 s66, s65, 0x80
	s_add_i32 s68, s62, 0xfffe0000
	s_mov_b32 m0, s53
	ds_read_b128 v[178:181], v156
	ds_read_b128 v[182:185], v156 offset:1024
	ds_read_b128 v[186:189], v156 offset:2048
	ds_read_b128 v[190:193], v156 offset:3072
	ds_read_b128 v[194:197], v156 offset:4096
	ds_read_b128 v[198:201], v156 offset:5120
	ds_read_b128 v[202:205], v156 offset:6144
	ds_read_b128 v[206:209], v156 offset:7168
	buffer_load_dwordx4 v1, s[8:11], s68 offen lds
	s_mov_b32 m0, s54
	s_nop 0
	buffer_load_dwordx4 v1, s[8:11], s62 offen lds
	s_waitcnt vmcnt(8)
	s_waitcnt lgkmcnt(0)
	s_barrier
	s_setprio 1
	s_waitcnt lgkmcnt(6)
	v_mfma_scale_f32_16x16x128_f8f6f4 v[134:137], v[106:113], v[178:185], v[134:137], v158, v157 op_sel_hi:[0,0,0]
	v_mfma_scale_f32_16x16x128_f8f6f4 v[130:133], v[138:145], v[178:185], v[130:133], v158, v157 op_sel_hi:[0,0,0]
	s_waitcnt lgkmcnt(4)
	v_mfma_scale_f32_16x16x128_f8f6f4 v[126:129], v[106:113], v[186:193], v[126:129], v158, v157 op_sel_hi:[0,0,0]
	v_mfma_scale_f32_16x16x128_f8f6f4 v[122:125], v[138:145], v[186:193], v[122:125], v158, v157 op_sel_hi:[0,0,0]
	s_waitcnt lgkmcnt(2)
	v_mfma_scale_f32_16x16x128_f8f6f4 v[118:121], v[106:113], v[194:201], v[118:121], v158, v157 op_sel_hi:[0,0,0]
	v_mfma_scale_f32_16x16x128_f8f6f4 v[114:117], v[138:145], v[194:201], v[114:117], v158, v157 op_sel_hi:[0,0,0]
	s_waitcnt lgkmcnt(0)
	v_mfma_scale_f32_16x16x128_f8f6f4 v[102:105], v[106:113], v[202:209], v[102:105], v158, v157 op_sel_hi:[0,0,0]
	v_mfma_scale_f32_16x16x128_f8f6f4 v[98:101], v[138:145], v[202:209], v[98:101], v158, v157 op_sel_hi:[0,0,0]
	s_setprio 0
	s_setprio 1
	v_mfma_scale_f32_16x16x128_f8f6f4 v[146:149], v[162:169], v[178:185], v[62:65], v158, v157 op_sel_hi:[0,0,0]
	v_mfma_scale_f32_16x16x128_f8f6f4 v[178:181], v[170:177], v[178:185], v[58:61], v158, v157 op_sel_hi:[0,0,0]
	v_mfma_scale_f32_16x16x128_f8f6f4 v[182:185], v[162:169], v[186:193], v[54:57], v158, v157 op_sel_hi:[0,0,0]
	v_mfma_scale_f32_16x16x128_f8f6f4 v[186:189], v[170:177], v[186:193], v[50:53], v158, v157 op_sel_hi:[0,0,0]
	v_mfma_scale_f32_16x16x128_f8f6f4 v[190:193], v[162:169], v[194:201], v[46:49], v158, v157 op_sel_hi:[0,0,0]
	v_mfma_scale_f32_16x16x128_f8f6f4 v[194:197], v[170:177], v[194:201], v[42:45], v158, v157 op_sel_hi:[0,0,0]
	v_mfma_scale_f32_16x16x128_f8f6f4 v[198:201], v[162:169], v[202:209], v[38:41], v158, v157 op_sel_hi:[0,0,0]
	v_mfma_scale_f32_16x16x128_f8f6f4 v[202:205], v[170:177], v[202:209], v[34:37], v158, v157 op_sel_hi:[0,0,0]
	s_setprio 0
	s_barrier
	s_mov_b32 m0, s23
	s_nop 3
	ds_read_b128 v[34:37], v156 offset:16384
	ds_read_b128 v[38:41], v156 offset:17408
	ds_read_b128 v[42:45], v156 offset:18432
	ds_read_b128 v[46:49], v156 offset:19456
	ds_read_b128 v[50:53], v156 offset:20480
	ds_read_b128 v[54:57], v156 offset:21504
	ds_read_b128 v[58:61], v156 offset:22528
	ds_read_b128 v[62:65], v156 offset:23552
	buffer_load_dwordx4 v152, s[8:11], s67 offen lds
	s_add_i32 s68, s67, 0x20000
	s_mov_b32 m0, s28
	s_nop 0
	buffer_load_dwordx4 v152, s[8:11], s68 offen lds
	s_add_i32 s68, s67, 0x40000
	s_mov_b32 m0, s29
	s_nop 0
	buffer_load_dwordx4 v152, s[8:11], s68 offen lds
	s_add_i32 s68, s67, 0x60000
	s_mov_b32 m0, s30
	s_nop 0
	buffer_load_dwordx4 v152, s[8:11], s68 offen lds
	s_waitcnt vmcnt(6)
	s_waitcnt lgkmcnt(0)
	s_barrier
	s_setprio 1
	s_waitcnt lgkmcnt(6)
	v_mfma_scale_f32_16x16x128_f8f6f4 v[94:97], v[106:113], v[34:41], v[94:97], v158, v157 op_sel_hi:[0,0,0]
	v_mfma_scale_f32_16x16x128_f8f6f4 v[90:93], v[138:145], v[34:41], v[90:93], v158, v157 op_sel_hi:[0,0,0]
	s_waitcnt lgkmcnt(4)
	v_mfma_scale_f32_16x16x128_f8f6f4 v[86:89], v[106:113], v[42:49], v[86:89], v158, v157 op_sel_hi:[0,0,0]
	v_mfma_scale_f32_16x16x128_f8f6f4 v[82:85], v[138:145], v[42:49], v[82:85], v158, v157 op_sel_hi:[0,0,0]
	s_waitcnt lgkmcnt(2)
	v_mfma_scale_f32_16x16x128_f8f6f4 v[78:81], v[106:113], v[50:57], v[78:81], v158, v157 op_sel_hi:[0,0,0]
	v_mfma_scale_f32_16x16x128_f8f6f4 v[74:77], v[138:145], v[50:57], v[74:77], v158, v157 op_sel_hi:[0,0,0]
	s_waitcnt lgkmcnt(0)
	v_mfma_scale_f32_16x16x128_f8f6f4 v[206:209], v[106:113], v[58:65], v[70:73], v158, v157 op_sel_hi:[0,0,0]
	v_mfma_scale_f32_16x16x128_f8f6f4 v[210:213], v[138:145], v[58:65], v[66:69], v158, v157 op_sel_hi:[0,0,0]
	s_setprio 0
	s_setprio 1
	v_mfma_scale_f32_16x16x128_f8f6f4 v[214:217], v[162:169], v[34:41], v[30:33], v158, v157 op_sel_hi:[0,0,0]
	v_mfma_scale_f32_16x16x128_f8f6f4 v[218:221], v[170:177], v[34:41], v[26:29], v158, v157 op_sel_hi:[0,0,0]
	v_mfma_scale_f32_16x16x128_f8f6f4 v[222:225], v[162:169], v[42:49], v[22:25], v158, v157 op_sel_hi:[0,0,0]
	v_mfma_scale_f32_16x16x128_f8f6f4 v[226:229], v[170:177], v[42:49], v[18:21], v158, v157 op_sel_hi:[0,0,0]
	v_mfma_scale_f32_16x16x128_f8f6f4 v[230:233], v[162:169], v[50:57], v[14:17], v158, v157 op_sel_hi:[0,0,0]
	v_mfma_scale_f32_16x16x128_f8f6f4 v[234:237], v[170:177], v[50:57], v[10:13], v158, v157 op_sel_hi:[0,0,0]
	v_mfma_scale_f32_16x16x128_f8f6f4 v[238:241], v[162:169], v[58:65], v[6:9], v158, v157 op_sel_hi:[0,0,0]
	v_mfma_scale_f32_16x16x128_f8f6f4 v[242:245], v[170:177], v[58:65], v[2:5], v158, v157 op_sel_hi:[0,0,0]
	s_setprio 0
	s_barrier
	s_nop 4
	ds_read_b128 v[2:5], v159
	ds_read_b128 v[6:9], v159 offset:1024
	ds_read_b128 v[10:13], v159 offset:2048
	ds_read_b128 v[14:17], v159 offset:3072
	ds_read_b128 v[106:109], v160
	ds_read_b128 v[110:113], v160 offset:1024
	ds_read_b128 v[138:141], v160 offset:2048
	ds_read_b128 v[142:145], v160 offset:3072
	s_mov_b32 m0, s34
	s_add_i32 s68, s65, 0x40000
	ds_read_b128 v[18:21], v156 offset:32768
	ds_read_b128 v[22:25], v156 offset:33792
	ds_read_b128 v[26:29], v156 offset:34816
	ds_read_b128 v[30:33], v156 offset:35840
	ds_read_b128 v[34:37], v156 offset:36864
	ds_read_b128 v[38:41], v156 offset:37888
	ds_read_b128 v[66:69], v156 offset:38912
	ds_read_b128 v[70:73], v156 offset:39936
	s_mov_b32 m0, s3
	s_nop 0
	buffer_load_dwordx4 v1, s[8:11], s65 offen lds
	s_add_i32 s68, s65, 0x20000
	s_mov_b32 m0, s31
	s_nop 0
	buffer_load_dwordx4 v1, s[8:11], s68 offen lds
	s_add_i32 s68, s65, 0x40000
	s_mov_b32 m0, s34
	s_nop 0
	buffer_load_dwordx4 v1, s[8:11], s68 offen lds
	s_add_i32 s68, s65, 0x60000
	s_mov_b32 m0, s35
	s_nop 0
	buffer_load_dwordx4 v1, s[8:11], s68 offen lds
	s_waitcnt vmcnt(8)
	s_waitcnt lgkmcnt(0)
	s_barrier
	s_setprio 1
	s_waitcnt lgkmcnt(6)
	v_mfma_scale_f32_16x16x128_f8f6f4 v[134:137], v[2:9], v[18:25], v[134:137], v158, v157 op_sel_hi:[0,0,0]
	v_mfma_scale_f32_16x16x128_f8f6f4 v[130:133], v[10:17], v[18:25], v[130:133], v158, v157 op_sel_hi:[0,0,0]
	s_waitcnt lgkmcnt(4)
	v_mfma_scale_f32_16x16x128_f8f6f4 v[126:129], v[2:9], v[26:33], v[126:129], v158, v157 op_sel_hi:[0,0,0]
	v_mfma_scale_f32_16x16x128_f8f6f4 v[122:125], v[10:17], v[26:33], v[122:125], v158, v157 op_sel_hi:[0,0,0]
	s_waitcnt lgkmcnt(2)
	v_mfma_scale_f32_16x16x128_f8f6f4 v[118:121], v[2:9], v[34:41], v[118:121], v158, v157 op_sel_hi:[0,0,0]
	v_mfma_scale_f32_16x16x128_f8f6f4 v[114:117], v[10:17], v[34:41], v[114:117], v158, v157 op_sel_hi:[0,0,0]
	s_waitcnt lgkmcnt(0)
	v_mfma_scale_f32_16x16x128_f8f6f4 v[102:105], v[2:9], v[66:73], v[102:105], v158, v157 op_sel_hi:[0,0,0]
	v_mfma_scale_f32_16x16x128_f8f6f4 v[98:101], v[10:17], v[66:73], v[98:101], v158, v157 op_sel_hi:[0,0,0]
	s_setprio 0
	s_setprio 1
	v_mfma_scale_f32_16x16x128_f8f6f4 v[62:65], v[106:113], v[18:25], v[146:149], v158, v157 op_sel_hi:[0,0,0]
	v_mfma_scale_f32_16x16x128_f8f6f4 v[58:61], v[138:145], v[18:25], v[178:181], v158, v157 op_sel_hi:[0,0,0]
	v_mfma_scale_f32_16x16x128_f8f6f4 v[54:57], v[106:113], v[26:33], v[182:185], v158, v157 op_sel_hi:[0,0,0]
	v_mfma_scale_f32_16x16x128_f8f6f4 v[50:53], v[138:145], v[26:33], v[186:189], v158, v157 op_sel_hi:[0,0,0]
	v_mfma_scale_f32_16x16x128_f8f6f4 v[46:49], v[106:113], v[34:41], v[190:193], v158, v157 op_sel_hi:[0,0,0]
	v_mfma_scale_f32_16x16x128_f8f6f4 v[42:45], v[138:145], v[34:41], v[194:197], v158, v157 op_sel_hi:[0,0,0]
	v_mfma_scale_f32_16x16x128_f8f6f4 v[38:41], v[106:113], v[66:73], v[198:201], v158, v157 op_sel_hi:[0,0,0]
	v_mfma_scale_f32_16x16x128_f8f6f4 v[34:37], v[138:145], v[66:73], v[202:205], v158, v157 op_sel_hi:[0,0,0]
	s_setprio 0
	s_barrier
	s_mov_b32 m0, s36
	s_add_i32 s68, s67, 0x80
	ds_read_b128 v[18:21], v156 offset:49152
	ds_read_b128 v[22:25], v156 offset:50176
	ds_read_b128 v[162:165], v156 offset:51200
	ds_read_b128 v[166:169], v156 offset:52224
	ds_read_b128 v[170:173], v156 offset:53248
	ds_read_b128 v[174:177], v156 offset:54272
	ds_read_b128 v[178:181], v156 offset:55296
	ds_read_b128 v[182:185], v156 offset:56320
	buffer_load_dwordx4 v152, s[8:11], s68 offen lds
	s_add_i32 s68, s67, 0x20080
	s_mov_b32 m0, s37
	s_add_i32 s65, s65, 0x20080
	buffer_load_dwordx4 v152, s[8:11], s68 offen lds
	s_add_i32 s68, s67, 0x40080
	s_mov_b32 m0, s40
	s_add_i32 s67, s67, 0x60080
	buffer_load_dwordx4 v152, s[8:11], s68 offen lds
	s_mov_b32 m0, s41
	s_nop 0
	buffer_load_dwordx4 v152, s[8:11], s67 offen lds
	s_mov_b32 m0, s38
	s_nop 0
	buffer_load_dwordx4 v1, s[8:11], s66 offen lds
	s_mov_b32 m0, s39
	s_nop 0
	buffer_load_dwordx4 v1, s[8:11], s65 offen lds
	s_waitcnt vmcnt(8)
	s_waitcnt lgkmcnt(0)
	s_barrier
	s_setprio 1
	s_waitcnt lgkmcnt(6)
	v_mfma_scale_f32_16x16x128_f8f6f4 v[94:97], v[2:9], v[18:25], v[94:97], v158, v157 op_sel_hi:[0,0,0]
	v_mfma_scale_f32_16x16x128_f8f6f4 v[90:93], v[10:17], v[18:25], v[90:93], v158, v157 op_sel_hi:[0,0,0]
	s_waitcnt lgkmcnt(4)
	v_mfma_scale_f32_16x16x128_f8f6f4 v[86:89], v[2:9], v[162:169], v[86:89], v158, v157 op_sel_hi:[0,0,0]
	v_mfma_scale_f32_16x16x128_f8f6f4 v[82:85], v[10:17], v[162:169], v[82:85], v158, v157 op_sel_hi:[0,0,0]
	s_waitcnt lgkmcnt(2)
	v_mfma_scale_f32_16x16x128_f8f6f4 v[78:81], v[2:9], v[170:177], v[78:81], v158, v157 op_sel_hi:[0,0,0]
	v_mfma_scale_f32_16x16x128_f8f6f4 v[74:77], v[10:17], v[170:177], v[74:77], v158, v157 op_sel_hi:[0,0,0]
	s_waitcnt lgkmcnt(0)
	v_mfma_scale_f32_16x16x128_f8f6f4 v[70:73], v[2:9], v[178:185], v[206:209], v158, v157 op_sel_hi:[0,0,0]
	v_mfma_scale_f32_16x16x128_f8f6f4 v[66:69], v[10:17], v[178:185], v[210:213], v158, v157 op_sel_hi:[0,0,0]
	s_setprio 0
	s_setprio 1
	v_mfma_scale_f32_16x16x128_f8f6f4 v[30:33], v[106:113], v[18:25], v[214:217], v158, v157 op_sel_hi:[0,0,0]
	v_mfma_scale_f32_16x16x128_f8f6f4 v[26:29], v[138:145], v[18:25], v[218:221], v158, v157 op_sel_hi:[0,0,0]
	v_mfma_scale_f32_16x16x128_f8f6f4 v[22:25], v[106:113], v[162:169], v[222:225], v158, v157 op_sel_hi:[0,0,0]
	v_mfma_scale_f32_16x16x128_f8f6f4 v[18:21], v[138:145], v[162:169], v[226:229], v158, v157 op_sel_hi:[0,0,0]
	v_mfma_scale_f32_16x16x128_f8f6f4 v[14:17], v[106:113], v[170:177], v[230:233], v158, v157 op_sel_hi:[0,0,0]
	v_mfma_scale_f32_16x16x128_f8f6f4 v[10:13], v[138:145], v[170:177], v[234:237], v158, v157 op_sel_hi:[0,0,0]
	v_mfma_scale_f32_16x16x128_f8f6f4 v[6:9], v[106:113], v[178:185], v[238:241], v158, v157 op_sel_hi:[0,0,0]
	v_mfma_scale_f32_16x16x128_f8f6f4 v[2:5], v[138:145], v[178:185], v[242:245], v158, v157 op_sel_hi:[0,0,0]
	s_setprio 0
	s_barrier
	s_add_i32 s64, s64, 2
	s_addk_i32 s62, 0x100
	s_addk_i32 s63, 0x100
	s_cmp_gt_u32 s64, 13
	s_cbranch_scc0 .LBB0_2336
	s_and_b64 vcc, exec, s[20:21]
	s_cbranch_vccz .LBB0_2339
	s_barrier
